# speedup vs baseline: 1.0008x; 1.0008x over previous
_Z8pam_mainPKDv4_jS1_S1_PKfS3_PDF16_Pf:
	s_load_dwordx8 s[4:11], s[0:1], 0x0
	s_load_dwordx4 s[12:15], s[0:1], 0x20
	s_load_dwordx2 s[16:17], s[0:1], 0x30
	v_and_b32_e32 v1, 63, v0
	v_lshrrev_b32_e32 v3, 6, v0
	v_lshlrev_b32_e32 v2, 4, v1
	v_lshlrev_b32_e32 v4, 2, v1
	v_readfirstlane_b32 s18, v3
	v_and_b32_e32 v3, 31, v1
	v_lshlrev_b32_e32 v5, 2, v3
	s_mul_i32 s19, s2, 54
	s_mul_i32 s20, s2, 3
	s_lshr_b32 s20, s20, 4
	s_mul_i32 s21, s20, 0x120
	s_sub_u32 s21, s19, s21
	s_cmp_ge_u32 s20, 24
	s_cselect_b32 s22, 0x120, 0
	s_add_u32 s22, s22, s21
	s_add_u32 s23, s20, 1
	s_cmp_ge_u32 s23, 24
	s_cselect_b32 s24, 0x120, 0
	s_sub_u32 s25, 0x120, s21
	s_cmp_lt_u32 s25, 54
	s_cselect_b32 s26, 1, 0
	s_mul_i32 s25, s25, 43
	s_lshr_b32 s25, s25, 8
	s_cmp_eq_u32 s26, 1
	s_cselect_b32 s25, s25, 100
	s_mov_b32 s29, s2
	s_mov_b32 s46, 0
	s_mov_b32 s47, 30720
	s_mov_b32 s48, 61440
	s_mov_b32 s27, 0
	s_mov_b32 s28, 1
	s_mul_i32 s30, s18, 0xd00
	s_add_u32 s30, s30, 92160
	v_add_u32_e32 v7, s30, v2
	v_mul_u32_u24_e32 v6, 0x68, v3
	v_lshrrev_b32_e32 v130, 2, v1
	v_and_b32_e32 v130, 8, v130
	v_add3_u32 v6, v6, v130, s30
	v_mov_b32_e32 v150, 0xf149f2ca
	s_cmp_ge_u32 s18, 4
	s_cbranch_scc0 .Lm_noprio
	s_setprio 1
